# silu(c) table fill: 18 loads per thread in flight (was one round trip each)
# speedup vs baseline: 1.0024x; 1.0024x over previous
.LBB0_7:
	s_or_b64 exec, exec, s[0:1]
	v_mov_b32_e32 v1, s60
	v_mov_b32_e32 v6, v0
	v_mov_b32_e32 v2, s61
	s_lshr_b32 s62, s4, 6
	s_movk_i32 s0, 0x2400
	v_readfirstlane_b32 s6, v1
	v_mov_b32_e32 v1, s62
	v_readfirstlane_b32 s7, v2
	v_readfirstlane_b32 s16, v1
	v_mov_b32_e32 v1, s58
	v_cmp_gt_i32_e32 vcc, s0, v6
	v_readfirstlane_b32 s18, v1
	v_mov_b32_e32 v1, s59
	v_ashrrev_i32_e32 v7, 31, v6
	v_readfirstlane_b32 s17, v1
	s_and_saveexec_b64 s[0:1], vcc
	s_cbranch_execz .LBB0_14
	s_add_i32 s11, 0, 0x25d18
	s_add_i32 s12, 0, 0x25d08
	v_mov_b32_e32 v4, s12
	ds_read_b64 v[8:9], v4
	v_mov_b32_e32 v4, s11
	ds_read_b64 v[10:11], v4
	v_lshlrev_b32_e32 v2, 2, v6
	v_lshl_add_u32 v1, v6, 2, 0
	v_add_u32_e32 v1, 0x11000, v1
	s_waitcnt lgkmcnt(0)
	v_readfirstlane_b32 s14, v8
	v_readfirstlane_b32 s15, v9
	v_readfirstlane_b32 s2, v10
	v_readfirstlane_b32 s3, v11
	s_nop 4
	global_load_dword v20, v2, s[14:15]
	s_add_u32 s14, s14, 0x800
	s_addc_u32 s15, s15, 0
	global_load_dword v21, v2, s[14:15]
	s_add_u32 s14, s14, 0x800
	s_addc_u32 s15, s15, 0
	global_load_dword v22, v2, s[14:15]
	s_add_u32 s14, s14, 0x800
	s_addc_u32 s15, s15, 0
	global_load_dword v23, v2, s[14:15]
	s_add_u32 s14, s14, 0x800
	s_addc_u32 s15, s15, 0
	global_load_dword v24, v2, s[14:15]
	s_add_u32 s14, s14, 0x800
	s_addc_u32 s15, s15, 0
	global_load_dword v25, v2, s[14:15]
	s_add_u32 s14, s14, 0x800
	s_addc_u32 s15, s15, 0
	global_load_dword v26, v2, s[14:15]
	s_add_u32 s14, s14, 0x800
	s_addc_u32 s15, s15, 0
	global_load_dword v27, v2, s[14:15]
	s_add_u32 s14, s14, 0x800
	s_addc_u32 s15, s15, 0
	global_load_dword v28, v2, s[14:15]
	s_add_u32 s14, s14, 0x800
	s_addc_u32 s15, s15, 0
	global_load_dword v29, v2, s[14:15]
	s_add_u32 s14, s14, 0x800
	s_addc_u32 s15, s15, 0
	global_load_dword v30, v2, s[14:15]
	s_add_u32 s14, s14, 0x800
	s_addc_u32 s15, s15, 0
	global_load_dword v31, v2, s[14:15]
	s_add_u32 s14, s14, 0x800
	s_addc_u32 s15, s15, 0
	global_load_dword v32, v2, s[14:15]
	s_add_u32 s14, s14, 0x800
	s_addc_u32 s15, s15, 0
	global_load_dword v33, v2, s[14:15]
	s_add_u32 s14, s14, 0x800
	s_addc_u32 s15, s15, 0
	global_load_dword v34, v2, s[14:15]
	s_add_u32 s14, s14, 0x800
	s_addc_u32 s15, s15, 0
	global_load_dword v35, v2, s[14:15]
	global_load_dword v36, v2, s[2:3]
	global_load_dword v37, v2, s[2:3] offset:2048
	s_waitcnt vmcnt(12)
	v_mul_f32_e32 v40, 0xbfb8aa3b, v20
	v_mul_f32_e32 v41, 0xbfb8aa3b, v21
	v_mul_f32_e32 v42, 0xbfb8aa3b, v22
	v_mul_f32_e32 v43, 0xbfb8aa3b, v23
	v_mul_f32_e32 v44, 0xbfb8aa3b, v24
	v_mul_f32_e32 v45, 0xbfb8aa3b, v25
	v_exp_f32_e32 v40, v40
	v_exp_f32_e32 v41, v41
	v_exp_f32_e32 v42, v42
	v_exp_f32_e32 v43, v43
	v_exp_f32_e32 v44, v44
	v_exp_f32_e32 v45, v45
	v_add_f32_e32 v40, 1.0, v40
	v_add_f32_e32 v41, 1.0, v41
	v_add_f32_e32 v42, 1.0, v42
	v_add_f32_e32 v43, 1.0, v43
	v_add_f32_e32 v44, 1.0, v44
	v_add_f32_e32 v45, 1.0, v45
	v_rcp_f32_e32 v40, v40
	v_rcp_f32_e32 v41, v41
	v_rcp_f32_e32 v42, v42
	v_rcp_f32_e32 v43, v43
	v_rcp_f32_e32 v44, v44
	v_rcp_f32_e32 v45, v45
	v_mul_f32_e32 v20, v20, v40
	v_mul_f32_e32 v21, v21, v41
	v_mul_f32_e32 v22, v22, v42
	v_mul_f32_e32 v23, v23, v43
	v_mul_f32_e32 v24, v24, v44
	v_mul_f32_e32 v25, v25, v45
	ds_write_b32 v1, v20 offset:0
	ds_write_b32 v1, v21 offset:2048
	ds_write_b32 v1, v22 offset:4096
	ds_write_b32 v1, v23 offset:6144
	ds_write_b32 v1, v24 offset:8192
	ds_write_b32 v1, v25 offset:10240
	s_waitcnt vmcnt(6)
	v_mul_f32_e32 v40, 0xbfb8aa3b, v26
	v_mul_f32_e32 v41, 0xbfb8aa3b, v27
	v_mul_f32_e32 v42, 0xbfb8aa3b, v28
	v_mul_f32_e32 v43, 0xbfb8aa3b, v29
	v_mul_f32_e32 v44, 0xbfb8aa3b, v30
	v_mul_f32_e32 v45, 0xbfb8aa3b, v31
	v_exp_f32_e32 v40, v40
	v_exp_f32_e32 v41, v41
	v_exp_f32_e32 v42, v42
	v_exp_f32_e32 v43, v43
	v_exp_f32_e32 v44, v44
	v_exp_f32_e32 v45, v45
	v_add_f32_e32 v40, 1.0, v40
	v_add_f32_e32 v41, 1.0, v41
	v_add_f32_e32 v42, 1.0, v42
	v_add_f32_e32 v43, 1.0, v43
	v_add_f32_e32 v44, 1.0, v44
	v_add_f32_e32 v45, 1.0, v45
	v_rcp_f32_e32 v40, v40
	v_rcp_f32_e32 v41, v41
	v_rcp_f32_e32 v42, v42
	v_rcp_f32_e32 v43, v43
	v_rcp_f32_e32 v44, v44
	v_rcp_f32_e32 v45, v45
	v_mul_f32_e32 v26, v26, v40
	v_mul_f32_e32 v27, v27, v41
	v_mul_f32_e32 v28, v28, v42
	v_mul_f32_e32 v29, v29, v43
	v_mul_f32_e32 v30, v30, v44
	v_mul_f32_e32 v31, v31, v45
	ds_write_b32 v1, v26 offset:12288
	ds_write_b32 v1, v27 offset:14336
	ds_write_b32 v1, v28 offset:16384
	ds_write_b32 v1, v29 offset:18432
	ds_write_b32 v1, v30 offset:20480
	ds_write_b32 v1, v31 offset:22528
	s_waitcnt vmcnt(0)
	v_mul_f32_e32 v40, 0xbfb8aa3b, v32
	v_mul_f32_e32 v41, 0xbfb8aa3b, v33
	v_mul_f32_e32 v42, 0xbfb8aa3b, v34
	v_mul_f32_e32 v43, 0xbfb8aa3b, v35
	v_mul_f32_e32 v44, 0xbfb8aa3b, v36
	v_mul_f32_e32 v45, 0xbfb8aa3b, v37
	v_exp_f32_e32 v40, v40
	v_exp_f32_e32 v41, v41
	v_exp_f32_e32 v42, v42
	v_exp_f32_e32 v43, v43
	v_exp_f32_e32 v44, v44
	v_exp_f32_e32 v45, v45
	v_add_f32_e32 v40, 1.0, v40
	v_add_f32_e32 v41, 1.0, v41
	v_add_f32_e32 v42, 1.0, v42
	v_add_f32_e32 v43, 1.0, v43
	v_add_f32_e32 v44, 1.0, v44
	v_add_f32_e32 v45, 1.0, v45
	v_rcp_f32_e32 v40, v40
	v_rcp_f32_e32 v41, v41
	v_rcp_f32_e32 v42, v42
	v_rcp_f32_e32 v43, v43
	v_rcp_f32_e32 v44, v44
	v_rcp_f32_e32 v45, v45
	v_mul_f32_e32 v32, v32, v40
	v_mul_f32_e32 v33, v33, v41
	v_mul_f32_e32 v34, v34, v42
	v_mul_f32_e32 v35, v35, v43
	v_mul_f32_e32 v36, v36, v44
	v_mul_f32_e32 v37, v37, v45
	ds_write_b32 v1, v32 offset:24576
	ds_write_b32 v1, v33 offset:26624
	ds_write_b32 v1, v34 offset:28672
	ds_write_b32 v1, v35 offset:30720
	ds_write_b32 v1, v36 offset:32768
	ds_write_b32 v1, v37 offset:34816
